# re-measure: MoE-up K-loop first iteration peeled (C=0 MFMAs), tok gather wait deferred
# speedup vs baseline: 1.0090x; 1.0021x over previous
.LBB0_1338:
	s_add_u32 s1, s72, 0x100
	s_addc_u32 s2, s73, 0
	s_add_u32 s14, s70, 0x80
	v_mov_b32_e32 v59, v187
	v_mov_b32_e32 v65, v187
	s_addc_u32 s15, s71, 0
	v_lshl_add_u64 v[74:75], s[14:15], 0, v[64:65]
	v_lshl_add_u64 v[76:77], s[14:15], 0, v[58:59]
	s_mov_b32 s34, -2
	s_mov_b64 s[40:41], 0
	s_add_u32 s14, s70, s40
	s_addc_u32 s15, s71, s41
	s_add_u32 s35, s14, 0x100
	s_addc_u32 s55, s15, 0
	s_add_u32 s61, s1, s40
	s_addc_u32 s69, s2, s41
	s_cmpk_eq_i32 s40, 0x700
	s_cselect_b64 vcc, -1, 0
	s_and_b64 s[14:15], vcc, exec
	s_cselect_b32 s15, s59, s55
	s_cselect_b32 s14, s58, s35
	s_cselect_b32 s73, s57, s69
	s_cselect_b32 s72, s56, s61
	s_add_i32 s35, 0, 0x11000
	v_add_u32_e32 v63, s35, v165
	s_add_i32 s55, 0, 0x15000
	ds_read_b128 v[78:81], v63
	ds_read_b128 v[154:157], v63 offset:1024
	ds_read_b128 v[158:161], v63 offset:2048
	ds_read_b128 v[172:175], v63 offset:3072
	v_add_u32_e32 v63, s55, v165
	ds_read_b128 v[176:179], v63
	ds_read_b128 v[180:183], v63 offset:1024
	ds_read_b128 v[196:199], v63 offset:2048
	ds_read_b128 v[200:203], v63 offset:3072
	v_cndmask_b32_e32 v186, v62, v171, vcc
	v_cndmask_b32_e32 v184, v60, v170, vcc
	v_cndmask_b32_e32 v59, v58, v168, vcc
	v_cndmask_b32_e32 v61, v64, v169, vcc
	v_lshl_add_u64 v[192:193], v[76:77], 0, s[40:41]
	s_add_i32 m0, s24, 0xd000
	ds_read_b128 v[204:207], v166 offset:4096
	ds_read_b128 v[208:211], v166 offset:5120
	ds_read_b128 v[212:215], v166 offset:6144
	ds_read_b128 v[216:219], v166 offset:7168
	ds_read_b128 v[220:223], v166 offset:8192
	ds_read_b128 v[240:243], v166 offset:9216
	ds_read_b128 v[244:247], v166 offset:10240
	ds_read_b128 v[248:251], v166 offset:11264
	global_load_lds_dwordx4 v[192:193], off
	v_lshl_add_u64 v[192:193], v[74:75], 0, s[40:41]
	s_add_i32 m0, s24, 0xf000
	s_nop 0
	global_load_lds_dwordx4 v[192:193], off
	s_waitcnt vmcnt(8)
	s_waitcnt lgkmcnt(0)
	s_barrier
	s_setprio 1
	s_waitcnt lgkmcnt(0)
	v_mfma_f32_16x16x32_bf16 v[142:145], v[78:81], v[204:207], 0
	v_mfma_f32_16x16x32_bf16 v[134:137], v[158:161], v[204:207], 0
	v_mfma_f32_16x16x32_bf16 v[126:129], v[78:81], v[212:215], 0
	v_mfma_f32_16x16x32_bf16 v[118:121], v[158:161], v[212:215], 0
	v_mfma_f32_16x16x32_bf16 v[110:113], v[78:81], v[220:223], 0
	v_mfma_f32_16x16x32_bf16 v[102:105], v[158:161], v[220:223], 0
	v_mfma_f32_16x16x32_bf16 v[94:97], v[78:81], v[244:247], 0
	v_mfma_f32_16x16x32_bf16 v[86:89], v[158:161], v[244:247], 0
	v_mfma_f32_16x16x32_bf16 v[142:145], v[154:157], v[208:211], v[142:145]
	v_mfma_f32_16x16x32_bf16 v[134:137], v[172:175], v[208:211], v[134:137]
	v_mfma_f32_16x16x32_bf16 v[126:129], v[154:157], v[216:219], v[126:129]
	v_mfma_f32_16x16x32_bf16 v[118:121], v[172:175], v[216:219], v[118:121]
	v_mfma_f32_16x16x32_bf16 v[110:113], v[154:157], v[240:243], v[110:113]
	v_mfma_f32_16x16x32_bf16 v[102:105], v[172:175], v[240:243], v[102:105]
	v_mfma_f32_16x16x32_bf16 v[94:97], v[154:157], v[248:251], v[94:97]
	v_mfma_f32_16x16x32_bf16 v[86:89], v[172:175], v[248:251], v[86:89]
	s_setprio 0
	s_setprio 1
	v_mfma_f32_16x16x32_bf16 v[138:141], v[176:179], v[204:207], 0
	v_mfma_f32_16x16x32_bf16 v[130:133], v[196:199], v[204:207], 0
	v_mfma_f32_16x16x32_bf16 v[122:125], v[176:179], v[212:215], 0
	v_mfma_f32_16x16x32_bf16 v[114:117], v[196:199], v[212:215], 0
	v_mfma_f32_16x16x32_bf16 v[106:109], v[176:179], v[220:223], 0
	v_mfma_f32_16x16x32_bf16 v[98:101], v[196:199], v[220:223], 0
	v_mfma_f32_16x16x32_bf16 v[90:93], v[176:179], v[244:247], 0
	v_mfma_f32_16x16x32_bf16 v[82:85], v[196:199], v[244:247], 0
	v_mfma_f32_16x16x32_bf16 v[138:141], v[180:183], v[208:211], v[138:141]
	v_mfma_f32_16x16x32_bf16 v[130:133], v[200:203], v[208:211], v[130:133]
	v_mfma_f32_16x16x32_bf16 v[122:125], v[180:183], v[216:219], v[122:125]
	v_mfma_f32_16x16x32_bf16 v[114:117], v[200:203], v[216:219], v[114:117]
	v_mfma_f32_16x16x32_bf16 v[106:109], v[180:183], v[240:243], v[106:109]
	v_mfma_f32_16x16x32_bf16 v[98:101], v[200:203], v[240:243], v[98:101]
	v_mfma_f32_16x16x32_bf16 v[90:93], v[180:183], v[248:251], v[90:93]
	v_mfma_f32_16x16x32_bf16 v[82:85], v[200:203], v[248:251], v[82:85]
	s_setprio 0
	s_barrier
	s_add_i32 s35, s35, s17
	v_lshl_add_u64 v[192:193], s[72:73], 0, v[148:149]
	s_mov_b32 m0, s35
	ds_read_b128 v[204:207], v166 offset:20480
	ds_read_b128 v[208:211], v166 offset:21504
	ds_read_b128 v[212:215], v166 offset:22528
	ds_read_b128 v[216:219], v166 offset:23552
	ds_read_b128 v[220:223], v166 offset:24576
	ds_read_b128 v[240:243], v166 offset:25600
	ds_read_b128 v[244:247], v166 offset:26624
	ds_read_b128 v[248:251], v166 offset:27648
	global_load_lds_dwordx4 v[192:193], off
	v_lshl_add_u64 v[224:225], v[192:193], 0, s[82:83]
	s_add_i32 m0, s35, 0x2000
	s_add_i32 s35, s55, s17
	global_load_lds_dwordx4 v[224:225], off
	v_lshl_add_u64 v[224:225], v[192:193], 0, s[64:65]
	s_mov_b32 m0, s35
	v_mov_b32_e32 v185, v187
	global_load_lds_dwordx4 v[224:225], off
	v_lshl_add_u64 v[224:225], v[192:193], 0, s[86:87]
	s_add_i32 m0, s35, 0x2000
	s_nop 0
	global_load_lds_dwordx4 v[224:225], off
	s_mov_b32 m0, s25
	v_lshl_add_u64 v[224:225], s[14:15], 0, v[186:187]
	global_load_lds_dwordx4 v186, s[14:15]
	s_mov_b32 m0, s28
	s_nop 0
	global_load_lds_dwordx4 v184, s[14:15]
	s_waitcnt vmcnt(8)
	s_waitcnt lgkmcnt(0)
	v_lshl_add_u64 v[184:185], s[14:15], 0, v[184:185]
	s_barrier
	s_cmp_lg_u64 s[38:39], 0
	s_cbranch_scc1 .Lup_tokskip
	v_lshlrev_b32_e32 v2, 10, v2
	v_lshlrev_b32_e32 v3, 10, v3
	v_lshlrev_b32_e32 v5, 10, v5
	v_lshlrev_b32_e32 v4, 10, v4
	v_add_lshl_u32 v168, v5, v164, 1
	v_add_lshl_u32 v170, v3, v164, 1
	v_add_lshl_u32 v171, v2, v164, 1
	v_add_lshl_u32 v169, v4, v164, 1
.Lup_tokskip:
	s_setprio 1
	s_waitcnt lgkmcnt(0)
	v_mfma_f32_16x16x32_bf16 v[70:73], v[78:81], v[204:207], 0
	v_mfma_f32_16x16x32_bf16 v[54:57], v[158:161], v[204:207], 0
	v_mfma_f32_16x16x32_bf16 v[46:49], v[78:81], v[212:215], 0
	v_mfma_f32_16x16x32_bf16 v[38:41], v[158:161], v[212:215], 0
	v_mfma_f32_16x16x32_bf16 v[30:33], v[78:81], v[220:223], 0
	v_mfma_f32_16x16x32_bf16 v[22:25], v[158:161], v[220:223], 0
	v_mfma_f32_16x16x32_bf16 v[14:17], v[78:81], v[244:247], 0
	v_mfma_f32_16x16x32_bf16 v[6:9], v[158:161], v[244:247], 0
	v_mfma_f32_16x16x32_bf16 v[70:73], v[154:157], v[208:211], v[70:73]
	v_mfma_f32_16x16x32_bf16 v[54:57], v[172:175], v[208:211], v[54:57]
	v_mfma_f32_16x16x32_bf16 v[46:49], v[154:157], v[216:219], v[46:49]
	v_mfma_f32_16x16x32_bf16 v[38:41], v[172:175], v[216:219], v[38:41]
	v_mfma_f32_16x16x32_bf16 v[30:33], v[154:157], v[240:243], v[30:33]
	v_mfma_f32_16x16x32_bf16 v[22:25], v[172:175], v[240:243], v[22:25]
	v_mfma_f32_16x16x32_bf16 v[14:17], v[154:157], v[248:251], v[14:17]
	v_mfma_f32_16x16x32_bf16 v[6:9], v[172:175], v[248:251], v[6:9]
	s_setprio 0
	s_setprio 1
	v_mfma_f32_16x16x32_bf16 v[66:69], v[176:179], v[204:207], 0
	v_mfma_f32_16x16x32_bf16 v[50:53], v[196:199], v[204:207], 0
	v_mfma_f32_16x16x32_bf16 v[42:45], v[176:179], v[212:215], 0
	v_mfma_f32_16x16x32_bf16 v[34:37], v[196:199], v[212:215], 0
	v_mfma_f32_16x16x32_bf16 v[26:29], v[176:179], v[220:223], 0
	v_mfma_f32_16x16x32_bf16 v[18:21], v[196:199], v[220:223], 0
	v_mfma_f32_16x16x32_bf16 v[10:13], v[176:179], v[244:247], 0
	v_mfma_f32_16x16x32_bf16 v[2:5], v[196:199], v[244:247], 0
	v_mfma_f32_16x16x32_bf16 v[66:69], v[180:183], v[208:211], v[66:69]
	v_mfma_f32_16x16x32_bf16 v[50:53], v[200:203], v[208:211], v[50:53]
	v_mfma_f32_16x16x32_bf16 v[42:45], v[180:183], v[216:219], v[42:45]
	v_mfma_f32_16x16x32_bf16 v[34:37], v[200:203], v[216:219], v[34:37]
	v_mfma_f32_16x16x32_bf16 v[26:29], v[180:183], v[240:243], v[26:29]
	v_mfma_f32_16x16x32_bf16 v[18:21], v[200:203], v[240:243], v[18:21]
	v_mfma_f32_16x16x32_bf16 v[10:13], v[180:183], v[248:251], v[10:13]
	v_mfma_f32_16x16x32_bf16 v[2:5], v[200:203], v[248:251], v[2:5]
	s_setprio 0
	s_barrier
	s_add_i32 s35, 0, 0x19000
	v_add_u32_e32 v63, s35, v165
	s_add_i32 s55, 0, 0x1d000
	ds_read_b128 v[78:81], v63
	ds_read_b128 v[154:157], v63 offset:1024
	ds_read_b128 v[158:161], v63 offset:2048
	ds_read_b128 v[172:175], v63 offset:3072
	v_add_u32_e32 v63, s55, v165
	ds_read_b128 v[176:179], v63
	ds_read_b128 v[180:183], v63 offset:1024
	ds_read_b128 v[196:199], v63 offset:2048
	ds_read_b128 v[200:203], v63 offset:3072
	s_mov_b32 m0, s29
	ds_read_b128 v[204:207], v166 offset:36864
	ds_read_b128 v[208:211], v166 offset:37888
	ds_read_b128 v[212:215], v166 offset:38912
	ds_read_b128 v[216:219], v166 offset:39936
	ds_read_b128 v[220:223], v166 offset:40960
	ds_read_b128 v[240:243], v166 offset:41984
	ds_read_b128 v[244:247], v166 offset:43008
	ds_read_b128 v[248:251], v166 offset:44032
	global_load_lds_dwordx4 v59, s[14:15]
	s_mov_b32 m0, s33
	s_nop 0
	global_load_lds_dwordx4 v61, s[14:15]
	s_waitcnt vmcnt(8)
	s_waitcnt lgkmcnt(0)
	s_barrier
	s_setprio 1
	s_waitcnt lgkmcnt(0)
	v_mfma_f32_16x16x32_bf16 v[142:145], v[78:81], v[204:207], v[142:145]
	v_mfma_f32_16x16x32_bf16 v[134:137], v[158:161], v[204:207], v[134:137]
	v_mfma_f32_16x16x32_bf16 v[126:129], v[78:81], v[212:215], v[126:129]
	v_mfma_f32_16x16x32_bf16 v[118:121], v[158:161], v[212:215], v[118:121]
	v_mfma_f32_16x16x32_bf16 v[110:113], v[78:81], v[220:223], v[110:113]
	v_mfma_f32_16x16x32_bf16 v[102:105], v[158:161], v[220:223], v[102:105]
	v_mfma_f32_16x16x32_bf16 v[94:97], v[78:81], v[244:247], v[94:97]
	v_mfma_f32_16x16x32_bf16 v[86:89], v[158:161], v[244:247], v[86:89]
	v_mfma_f32_16x16x32_bf16 v[142:145], v[154:157], v[208:211], v[142:145]
	v_mfma_f32_16x16x32_bf16 v[134:137], v[172:175], v[208:211], v[134:137]
	v_mfma_f32_16x16x32_bf16 v[126:129], v[154:157], v[216:219], v[126:129]
	v_mfma_f32_16x16x32_bf16 v[118:121], v[172:175], v[216:219], v[118:121]
	v_mfma_f32_16x16x32_bf16 v[110:113], v[154:157], v[240:243], v[110:113]
	v_mfma_f32_16x16x32_bf16 v[102:105], v[172:175], v[240:243], v[102:105]
	v_mfma_f32_16x16x32_bf16 v[94:97], v[154:157], v[248:251], v[94:97]
	v_mfma_f32_16x16x32_bf16 v[86:89], v[172:175], v[248:251], v[86:89]
	s_setprio 0
	s_setprio 1
	v_mfma_f32_16x16x32_bf16 v[138:141], v[176:179], v[204:207], v[138:141]
	v_mfma_f32_16x16x32_bf16 v[130:133], v[196:199], v[204:207], v[130:133]
	v_mfma_f32_16x16x32_bf16 v[122:125], v[176:179], v[212:215], v[122:125]
	v_mfma_f32_16x16x32_bf16 v[114:117], v[196:199], v[212:215], v[114:117]
	v_mfma_f32_16x16x32_bf16 v[106:109], v[176:179], v[220:223], v[106:109]
	v_mfma_f32_16x16x32_bf16 v[98:101], v[196:199], v[220:223], v[98:101]
	v_mfma_f32_16x16x32_bf16 v[90:93], v[176:179], v[244:247], v[90:93]
	v_mfma_f32_16x16x32_bf16 v[82:85], v[196:199], v[244:247], v[82:85]
	v_mfma_f32_16x16x32_bf16 v[138:141], v[180:183], v[208:211], v[138:141]
	v_mfma_f32_16x16x32_bf16 v[130:133], v[200:203], v[208:211], v[130:133]
	v_mfma_f32_16x16x32_bf16 v[122:125], v[180:183], v[216:219], v[122:125]
	v_mfma_f32_16x16x32_bf16 v[114:117], v[200:203], v[216:219], v[114:117]
	v_mfma_f32_16x16x32_bf16 v[106:109], v[180:183], v[240:243], v[106:109]
	v_mfma_f32_16x16x32_bf16 v[98:101], v[200:203], v[240:243], v[98:101]
	v_mfma_f32_16x16x32_bf16 v[90:93], v[180:183], v[248:251], v[90:93]
	v_mfma_f32_16x16x32_bf16 v[82:85], v[200:203], v[248:251], v[82:85]
	s_setprio 0
	s_barrier
	s_add_i32 s14, s35, s17
	v_lshl_add_u64 v[230:231], v[192:193], 0, s[92:93]
	s_mov_b32 m0, s14
	ds_read_b128 v[204:207], v166 offset:53248
	ds_read_b128 v[208:211], v166 offset:54272
	ds_read_b128 v[212:215], v166 offset:55296
	ds_read_b128 v[216:219], v166 offset:56320
	ds_read_b128 v[220:223], v166 offset:57344
	ds_read_b128 v[240:243], v166 offset:58368
	ds_read_b128 v[244:247], v166 offset:59392
	ds_read_b128 v[248:251], v166 offset:60416
	global_load_lds_dwordx4 v[230:231], off
	v_lshl_add_u64 v[230:231], v[192:193], 0, s[4:5]
	s_add_i32 m0, s14, 0x2000
	s_add_i32 s14, s55, s17
	global_load_lds_dwordx4 v[230:231], off
	v_lshl_add_u64 v[230:231], v[192:193], 0, s[6:7]
	s_mov_b32 m0, s14
	v_lshl_add_u64 v[192:193], v[192:193], 0, s[8:9]
	global_load_lds_dwordx4 v[230:231], off
	s_add_i32 m0, s14, 0x2000
	v_lshl_add_u64 v[184:185], v[184:185], 0, s[92:93]
	global_load_lds_dwordx4 v[192:193], off
	v_lshl_add_u64 v[192:193], v[224:225], 0, s[92:93]
	s_mov_b32 m0, s80
	s_nop 0
	global_load_lds_dwordx4 v[192:193], off
	s_mov_b32 m0, s81
	s_nop 0
	global_load_lds_dwordx4 v[184:185], off
	s_waitcnt vmcnt(8)
	s_waitcnt lgkmcnt(0)
	s_barrier
	s_setprio 1
	s_waitcnt lgkmcnt(0)
	v_mfma_f32_16x16x32_bf16 v[70:73], v[78:81], v[204:207], v[70:73]
	v_mfma_f32_16x16x32_bf16 v[54:57], v[158:161], v[204:207], v[54:57]
	v_mfma_f32_16x16x32_bf16 v[46:49], v[78:81], v[212:215], v[46:49]
	v_mfma_f32_16x16x32_bf16 v[38:41], v[158:161], v[212:215], v[38:41]
	v_mfma_f32_16x16x32_bf16 v[30:33], v[78:81], v[220:223], v[30:33]
	v_mfma_f32_16x16x32_bf16 v[22:25], v[158:161], v[220:223], v[22:25]
	v_mfma_f32_16x16x32_bf16 v[14:17], v[78:81], v[244:247], v[14:17]
	v_mfma_f32_16x16x32_bf16 v[6:9], v[158:161], v[244:247], v[6:9]
	v_mfma_f32_16x16x32_bf16 v[70:73], v[154:157], v[208:211], v[70:73]
	v_mfma_f32_16x16x32_bf16 v[54:57], v[172:175], v[208:211], v[54:57]
	v_mfma_f32_16x16x32_bf16 v[46:49], v[154:157], v[216:219], v[46:49]
	v_mfma_f32_16x16x32_bf16 v[38:41], v[172:175], v[216:219], v[38:41]
	v_mfma_f32_16x16x32_bf16 v[30:33], v[154:157], v[240:243], v[30:33]
	v_mfma_f32_16x16x32_bf16 v[22:25], v[172:175], v[240:243], v[22:25]
	v_mfma_f32_16x16x32_bf16 v[14:17], v[154:157], v[248:251], v[14:17]
	v_mfma_f32_16x16x32_bf16 v[6:9], v[172:175], v[248:251], v[6:9]
	s_setprio 0
	s_setprio 1
	v_mfma_f32_16x16x32_bf16 v[66:69], v[176:179], v[204:207], v[66:69]
	v_mfma_f32_16x16x32_bf16 v[50:53], v[196:199], v[204:207], v[50:53]
	v_mfma_f32_16x16x32_bf16 v[42:45], v[176:179], v[212:215], v[42:45]
	v_mfma_f32_16x16x32_bf16 v[34:37], v[196:199], v[212:215], v[34:37]
	v_mfma_f32_16x16x32_bf16 v[26:29], v[176:179], v[220:223], v[26:29]
	v_mfma_f32_16x16x32_bf16 v[18:21], v[196:199], v[220:223], v[18:21]
	v_mfma_f32_16x16x32_bf16 v[10:13], v[176:179], v[244:247], v[10:13]
	v_mfma_f32_16x16x32_bf16 v[2:5], v[196:199], v[244:247], v[2:5]
	v_mfma_f32_16x16x32_bf16 v[66:69], v[180:183], v[208:211], v[66:69]
	v_mfma_f32_16x16x32_bf16 v[50:53], v[200:203], v[208:211], v[50:53]
	v_mfma_f32_16x16x32_bf16 v[42:45], v[180:183], v[216:219], v[42:45]
	v_mfma_f32_16x16x32_bf16 v[34:37], v[200:203], v[216:219], v[34:37]
	v_mfma_f32_16x16x32_bf16 v[26:29], v[180:183], v[240:243], v[26:29]
	v_mfma_f32_16x16x32_bf16 v[18:21], v[200:203], v[240:243], v[18:21]
	v_mfma_f32_16x16x32_bf16 v[10:13], v[180:183], v[248:251], v[10:13]
	v_mfma_f32_16x16x32_bf16 v[2:5], v[200:203], v[248:251], v[2:5]
	s_setprio 0
	s_barrier
	s_add_i32 s34, s34, 2
	s_add_u32 s40, s40, 0x100
	s_addc_u32 s41, s41, 0
